# conv_queue: transposition LDS reads batched (8 reads, 2 waits), queue-ticket atomic issued one iteration ahead so its latency overlaps the tile work
# baseline (speedup 1.0000x reference)
.LBB0_1821:
	s_or_b64 exec, exec, s[18:19]
	s_and_saveexec_b64 s[18:19], s[0:1]
	s_cbranch_execz .LBB0_1912
	v_readlane_b32 s0, v253, 55
	s_lshl_b32 s63, s0, 22
	s_lshl_b32 s64, s0, 2
	s_lshl_b32 s65, s0, 24
	s_lshl_b32 s50, s0, 25
	s_movk_i32 s0, 0x104
	v_ashrrev_i32_e32 v4, 6, v20
	v_mul_lo_u32 v6, v37, s0
	v_bfi_b32 v4, -4, v4, v20
	s_movk_i32 s0, 0x820
	v_lshlrev_b32_e32 v44, 3, v4
	v_mul_lo_u32 v7, v4, s0
	v_add_u32_e32 v4, 0x200, v20
	v_ashrrev_i32_e32 v4, 6, v4
	v_bfe_u32 v51, v20, 2, 6
	v_bfi_b32 v4, -4, v4, v20
	v_lshl_add_u32 v2, v36, 2, 0
	v_lshl_add_u32 v5, v51, 2, 0
	v_lshlrev_b32_e32 v46, 3, v4
	v_mul_lo_u32 v8, v4, s0
	s_add_u32 s8, s8, s24
	v_mov_b32_e32 v4, 0
	v_add_u32_e32 v48, 32, v37
	v_add_u32_e32 v49, 64, v37
	v_add_u32_e32 v50, 0x60, v37
	v_ashrrev_i32_e32 v45, 31, v44
	v_ashrrev_i32_e32 v47, 31, v46
	s_addc_u32 s9, s9, s25
	s_mov_b32 s66, 0
	s_mov_b64 s[20:21], 0
	v_add_u32_e32 v52, v2, v6
	v_add_u32_e32 v53, v5, v7
	v_add_u32_e32 v54, v5, v8
	v_mov_b32_e32 v5, v4
	v_mov_b32_e32 v6, v4
	v_mov_b32_e32 v7, v4
	v_mov_b32_e32 v8, v4
	v_mov_b32_e32 v9, v4
	v_mov_b32_e32 v10, v4
	v_mov_b32_e32 v11, v4
	v_mov_b32_e32 v20, v4
	v_mov_b32_e32 v21, v4
	v_mov_b32_e32 v22, v4
	v_mov_b32_e32 v23, v4
	v_mov_b32_e32 v24, v4
	v_mov_b32_e32 v25, v4
	v_mov_b32_e32 v26, v4
	v_mov_b32_e32 v27, v4
	s_mov_b64 s[100:101], exec
	s_and_b64 exec, exec, vcc
	s_cbranch_execz .Lmy_cq_skip0
	v_mov_b32_e32 v55, 1
	global_atomic_add v55, v3, v55, s[14:15] offset:3072 sc0
.Lmy_cq_skip0:
	s_mov_b64 exec, s[100:101]
	s_branch .LBB0_1826

.LBB0_1825:
	s_or_b64 exec, exec, s[22:23]
	s_and_b64 s[0:1], exec, s[0:1]
	v_add_u32_e32 v18, v39, v51
	s_or_b64 s[20:21], s[0:1], s[20:21]
	v_mad_u64_u32 v[12:13], s[0:1], v42, v18, 0
	v_mov_b32_e32 v2, v13
	v_mad_u64_u32 v[18:19], s[0:1], v43, v18, v[2:3]
	v_mov_b32_e32 v13, v18
	v_add_u32_e32 v2, 0x400, v53
	v_add_u32_e32 v196, 0x400, v54
	ds_read2_b32 v[180:181], v53 offset1:65
	ds_read2_b32 v[182:183], v53 offset0:130 offset1:195
	ds_read2_b32 v[184:185], v2 offset0:4 offset1:69
	ds_read2_b32 v[186:187], v2 offset0:134 offset1:199
	ds_read2_b32 v[188:189], v54 offset1:65
	ds_read2_b32 v[190:191], v54 offset0:130 offset1:195
	ds_read2_b32 v[192:193], v196 offset0:4 offset1:69
	ds_read2_b32 v[194:195], v196 offset0:134 offset1:199
	v_lshl_add_u64 v[12:13], v[12:13], 1, v[40:41]
	v_ashrrev_i32_e32 v39, 31, v38
	v_lshl_add_u64 v[12:13], v[38:39], 1, v[12:13]
	v_mov_b32_e32 v38, v33
	v_mov_b32_e32 v39, v32
	v_mov_b64_e32 v[42:43], v[16:17]
	v_mov_b64_e32 v[40:41], v[14:15]
	v_lshl_add_u64 v[18:19], v[44:45], 1, v[12:13]
	v_lshl_add_u64 v[12:13], v[46:47], 1, v[12:13]
	s_waitcnt lgkmcnt(4)
	v_cvt_pk_bf16_f32 v28, v180, v181
	v_cvt_pk_bf16_f32 v29, v182, v183
	v_cvt_pk_bf16_f32 v30, v184, v185
	v_cvt_pk_bf16_f32 v31, v186, v187
	global_store_dwordx4 v[18:19], v[28:31], off
	s_waitcnt lgkmcnt(0)
	v_cvt_pk_bf16_f32 v200, v188, v189
	v_cvt_pk_bf16_f32 v201, v190, v191
	v_cvt_pk_bf16_f32 v202, v192, v193
	v_cvt_pk_bf16_f32 v203, v194, v195
	global_store_dwordx4 v[12:13], v[200:203], off
	s_waitcnt vmcnt(2)
	v_pk_mul_f32 v[4:5], v[4:5], v[238:239] op_sel_hi:[1,0]
	v_pk_mul_f32 v[6:7], v[6:7], v[238:239] op_sel_hi:[1,0]
	v_pk_mul_f32 v[8:9], v[8:9], v[240:241] op_sel_hi:[1,0]
	v_pk_mul_f32 v[10:11], v[10:11], v[240:241] op_sel_hi:[1,0]
	v_pk_mul_f32 v[20:21], v[20:21], v[242:243] op_sel_hi:[1,0]
	v_pk_mul_f32 v[22:23], v[22:23], v[242:243] op_sel_hi:[1,0]
	v_pk_mul_f32 v[24:25], v[24:25], v[244:245] op_sel_hi:[1,0]
	v_pk_mul_f32 v[26:27], v[26:27], v[244:245] op_sel_hi:[1,0]
	v_mov_b32_e32 v16, v4
	v_mov_b32_e32 v17, v5
	v_mov_b32_e32 v14, v10
	v_mov_b32_e32 v15, v11
	v_mov_b32_e32 v32, v20
	v_mov_b32_e32 v33, v21
	v_mov_b32_e32 v34, v22
	v_mov_b32_e32 v35, v23
	v_mov_b32_e32 v18, v6
	v_mov_b32_e32 v19, v7
	v_mov_b32_e32 v12, v8
	v_mov_b32_e32 v13, v9
	v_mov_b32_e32 v28, v24
	v_mov_b32_e32 v29, v25
	v_mov_b32_e32 v30, v26
	v_mov_b32_e32 v31, v27
	s_barrier
	s_andn2_b64 exec, exec, s[20:21]
	s_cbranch_execz .LBB0_1912
.LBB0_1826:
	s_xor_b32 s66, s66, 1
	s_and_saveexec_b64 s[2:3], vcc
	s_cbranch_execz .LBB0_1830
	s_lshl_b32 s0, s66, 2
	s_add_i32 s0, s0, 0
	s_add_i32 s0, s0, 0x8200
	v_mov_b32_e32 v56, s0
	v_readlane_b32 s0, v252, 6
	v_readlane_b32 s1, v252, 7
	s_waitcnt vmcnt(0)
	v_readfirstlane_b32 s0, v55
	v_mov_b32_e32 v57, s1
	s_nop 0
	v_mov_b32_e32 v2, s0
	flat_store_dword v[56:57], v2 sc0 sc1
	s_waitcnt vmcnt(0)
.LBB0_1830:
	s_or_b64 exec, exec, s[2:3]
	v_add_u32_e32 v2, 0x2080, v52
	s_lshl_b32 s0, s66, 2
	s_waitcnt vmcnt(0)
	ds_write2_b32 v52, v16, v17 offset1:1
	ds_write2_b32 v52, v18, v19 offset0:2 offset1:3
	ds_write2_b32 v2, v12, v13 offset1:1
	v_add_u32_e32 v2, 0x2088, v52
	s_add_i32 s0, s0, 0
	ds_write2_b32 v2, v14, v15 offset1:1
	v_add_u32_e32 v2, 0x4100, v52
	s_add_i32 s0, s0, 0x8200
	ds_write2_b32 v2, v32, v33 offset1:1
	v_add_u32_e32 v2, 0x4108, v52
	v_mov_b32_e32 v12, s0
	v_readlane_b32 s0, v252, 6
	ds_write2_b32 v2, v34, v35 offset1:1
	v_add_u32_e32 v2, 0x6180, v52
	v_readlane_b32 s1, v252, 7
	ds_write2_b32 v2, v28, v29 offset1:1
	v_add_u32_e32 v2, 0x6188, v52
	v_mov_b32_e32 v13, s1
	ds_write2_b32 v2, v30, v31 offset1:1
	s_waitcnt lgkmcnt(0)
	s_barrier
	flat_load_dword v30, v[12:13] sc0 sc1
	s_waitcnt vmcnt(0)
	s_mov_b64 s[100:101], exec
	s_and_b64 exec, exec, vcc
	s_cbranch_execz .Lmy_cq_skip1
	v_mov_b32_e32 v55, 1
	global_atomic_add v55, v3, v55, s[14:15] offset:3072 sc0
.Lmy_cq_skip1:
	s_mov_b64 exec, s[100:101]
	v_mov_b64_e32 v[16:17], 0
	v_mov_b32_e32 v33, 0
	v_mov_b32_e32 v32, 0
	v_mov_b64_e32 v[14:15], 0
	s_waitcnt lgkmcnt(0)
	v_cmp_gt_i32_e64 s[2:3], s62, v30
	v_cmp_le_i32_e64 s[0:1], s62, v30
	s_and_saveexec_b64 s[22:23], s[2:3]
	s_cbranch_execz .LBB0_1825
	s_movk_i32 s2, 0xbff
	v_cmp_lt_i32_e64 s[2:3], s2, v30
	s_and_saveexec_b64 s[4:5], s[2:3]
	s_xor_b64 s[4:5], exec, s[4:5]
	s_cbranch_execz .LBB0_1891
	s_movk_i32 s2, 0xdff
	v_cmp_lt_u32_e64 s[2:3], s2, v30
	s_and_saveexec_b64 s[26:27], s[2:3]
	s_xor_b64 s[26:27], exec, s[26:27]
	s_cbranch_execz .LBB0_1888
	s_movk_i32 s2, 0xebf
	v_cmp_lt_u32_e64 s[2:3], s2, v30
	s_and_saveexec_b64 s[28:29], s[2:3]
	s_xor_b64 s[28:29], exec, s[28:29]
	s_cbranch_execz .LBB0_1885
	s_movk_i32 s2, 0xf3f
	v_cmp_lt_u32_e64 s[2:3], s2, v30
	s_and_saveexec_b64 s[30:31], s[2:3]
	s_xor_b64 s[30:31], exec, s[30:31]
	s_cbranch_execz .LBB0_1882
	v_add_u16_e32 v2, 0xf0c0, v30
	v_mul_u32_u24_e32 v4, 0xe38f, v2
	v_lshrrev_b32_e32 v4, 22, v4
	v_mul_lo_u16_e32 v5, 0x48, v4
	v_sub_u16_e32 v5, v2, v5
	v_lshlrev_b16_e32 v32, 6, v5
	v_or_b32_e32 v2, v36, v32
	v_cmp_lt_u16_e64 s[2:3], 17, v5
	s_and_saveexec_b64 s[34:35], s[2:3]
	s_cbranch_execz .LBB0_1881
	v_cmp_lt_u16_e64 s[2:3], 23, v5
	s_and_saveexec_b64 s[36:37], s[2:3]
	s_xor_b64 s[36:37], exec, s[36:37]
	s_cbranch_execz .LBB0_1878
	v_cmp_lt_u16_e64 s[2:3], 29, v5
	s_and_saveexec_b64 s[38:39], s[2:3]
	s_xor_b64 s[38:39], exec, s[38:39]
	s_cbranch_execz .LBB0_1875
	v_cmp_lt_u16_e64 s[2:3], 35, v5
	s_and_saveexec_b64 s[40:41], s[2:3]
	s_xor_b64 s[40:41], exec, s[40:41]
	s_cbranch_execz .LBB0_1872
	v_cmp_lt_u16_e64 s[2:3], 41, v5
	s_and_saveexec_b64 s[42:43], s[2:3]
	s_xor_b64 s[42:43], exec, s[42:43]
	s_cbranch_execz .LBB0_1869
	v_cmp_lt_u16_e64 s[2:3], 47, v5
	s_and_saveexec_b64 s[44:45], s[2:3]
	s_xor_b64 s[44:45], exec, s[44:45]
	s_cbranch_execz .LBB0_1866
	v_cmp_lt_u16_e64 s[2:3], 53, v5
	s_and_saveexec_b64 s[46:47], s[2:3]
	s_xor_b64 s[46:47], exec, s[46:47]
	s_cbranch_execz .LBB0_1863
	v_cmp_lt_u16_e64 s[2:3], 59, v5
	s_and_saveexec_b64 s[48:49], s[2:3]
	s_xor_b64 s[48:49], exec, s[48:49]
	s_cbranch_execz .LBB0_1860
	s_movk_i32 s2, 0x41
	v_cmp_lt_u16_e64 s[2:3], s2, v5
	s_and_saveexec_b64 s[52:53], s[2:3]
	s_xor_b64 s[52:53], exec, s[52:53]
	s_cbranch_execz .LBB0_1857
	s_movk_i32 s2, 0x43
	v_cmp_lt_u16_e64 s[2:3], s2, v5
	s_and_saveexec_b64 s[54:55], s[2:3]
	s_xor_b64 s[54:55], exec, s[54:55]
	s_cbranch_execz .LBB0_1854
	s_movk_i32 s2, 0x111f
	v_cmp_lt_u32_e64 s[2:3], s2, v2
	s_and_saveexec_b64 s[56:57], s[2:3]
	s_xor_b64 s[56:57], exec, s[56:57]
	s_cbranch_execz .LBB0_1851
	s_movk_i32 s2, 0x112f
	v_cmp_lt_u32_e64 s[2:3], s2, v2
	s_and_saveexec_b64 s[58:59], s[2:3]
	s_xor_b64 s[58:59], exec, s[58:59]
	s_movk_i32 s2, 0x1134
	v_add_u32_e32 v5, 0xfffff880, v2
	v_cmp_gt_u32_e64 s[2:3], s2, v2
	s_nop 1
	v_cndmask_b32_e64 v2, -1, v5, s[2:3]
	s_andn2_saveexec_b64 s[2:3], s[58:59]
	v_add_u32_e32 v2, 0xfffff360, v2
	s_or_b64 exec, exec, s[2:3]

	.amdhsa_kernel _Z4mega6Params
		.amdhsa_group_segment_fixed_size 0
		.amdhsa_private_segment_fixed_size 0
		.amdhsa_kernarg_size 640
		.amdhsa_user_sgpr_count 2
		.amdhsa_user_sgpr_dispatch_ptr 0
		.amdhsa_user_sgpr_queue_ptr 0
		.amdhsa_user_sgpr_kernarg_segment_ptr 1
		.amdhsa_user_sgpr_dispatch_id 0
		.amdhsa_user_sgpr_kernarg_preload_length 0
		.amdhsa_user_sgpr_kernarg_preload_offset 0
		.amdhsa_user_sgpr_private_segment_size 0
		.amdhsa_uses_dynamic_stack 0
		.amdhsa_enable_private_segment 0
		.amdhsa_system_sgpr_workgroup_id_x 1
		.amdhsa_system_sgpr_workgroup_id_y 0
		.amdhsa_system_sgpr_workgroup_id_z 0
		.amdhsa_system_sgpr_workgroup_info 0
		.amdhsa_system_vgpr_workitem_id 0
		.amdhsa_next_free_vgpr 256
		.amdhsa_next_free_sgpr 102
		.amdhsa_accum_offset 256
		.amdhsa_reserve_vcc 1
		.amdhsa_float_round_mode_32 0
		.amdhsa_float_round_mode_16_64 0
		.amdhsa_float_denorm_mode_32 3
		.amdhsa_float_denorm_mode_16_64 3
		.amdhsa_dx10_clamp 1
		.amdhsa_ieee_mode 1
		.amdhsa_fp16_overflow 0
		.amdhsa_tg_split 0
		.amdhsa_exception_fp_ieee_invalid_op 0
		.amdhsa_exception_fp_denorm_src 0
		.amdhsa_exception_fp_ieee_div_zero 0
		.amdhsa_exception_fp_ieee_overflow 0
		.amdhsa_exception_fp_ieee_underflow 0
		.amdhsa_exception_fp_ieee_inexact 0
		.amdhsa_exception_int_div_zero 0
	.end_amdhsa_kernel

amdhsa.kernels:
  - .agpr_count:     0
    .args:
      - .offset:         0
        .size:           384
        .value_kind:     by_value
      - .offset:         384
        .size:           4
        .value_kind:     hidden_block_count_x
      - .offset:         388
        .size:           4
        .value_kind:     hidden_block_count_y
      - .offset:         392
        .size:           4
        .value_kind:     hidden_block_count_z
      - .offset:         396
        .size:           2
        .value_kind:     hidden_group_size_x
      - .offset:         398
        .size:           2
        .value_kind:     hidden_group_size_y
      - .offset:         400
        .size:           2
        .value_kind:     hidden_group_size_z
      - .offset:         402
        .size:           2
        .value_kind:     hidden_remainder_x
      - .offset:         404
        .size:           2
        .value_kind:     hidden_remainder_y
      - .offset:         406
        .size:           2
        .value_kind:     hidden_remainder_z
      - .offset:         424
        .size:           8
        .value_kind:     hidden_global_offset_x
      - .offset:         432
        .size:           8
        .value_kind:     hidden_global_offset_y
      - .offset:         440
        .size:           8
        .value_kind:     hidden_global_offset_z
      - .offset:         448
        .size:           2
        .value_kind:     hidden_grid_dims
      - .offset:         504
        .size:           4
        .value_kind:     hidden_dynamic_lds_size
    .group_segment_fixed_size: 0
    .kernarg_segment_align: 8
    .kernarg_segment_size: 640
    .language:       OpenCL C
    .language_version:
      - 2
      - 0
    .max_flat_workgroup_size: 512
    .name:           _Z4mega6Params
    .private_segment_fixed_size: 0
    .sgpr_count:     108
    .sgpr_spill_count: 254
    .symbol:         _Z4mega6Params.kd
    .uniform_work_group_size: 1
    .uses_dynamic_stack: false
    .vgpr_count:     256
    .vgpr_spill_count: 0
    .wavefront_size: 64
